# baseline (speedup 1.0000x reference)
_Z11center_mainPKfPKcS0_Pf:
	s_load_dwordx4 s[4:7], s[0:1], 0x0
	s_load_dwordx4 s[8:11], s[0:1], 0x10
	s_and_b32 s3, s2, 7
	s_lshr_b32 s12, s2, 3
	s_mov_b32 s30, s2
	v_lshrrev_b32_e32 v1, 6, v0
	v_and_b32_e32 v2, 63, v0
	v_bfe_u32 v3, v0, 3, 3
	v_and_b32_e32 v4, 7, v0
	v_lshrrev_b32_e32 v5, 7, v0
	v_bfe_u32 v6, v0, 6, 1
	v_lshl_or_b32 v7, v5, 3, v3
	v_lshlrev_b32_e32 v8, 10, v7
	v_lshl_or_b32 v8, v6, 9, v8
	v_lshl_or_b32 v226, v4, 4, v8
	v_lshlrev_b32_e32 v17, 15, v1
	v_lshl_or_b32 v227, v2, 5, v17
	v_lshlrev_b32_e32 v237, 3, v0
	s_lshl_b32 s13, s3, 22
	s_lshl_b32 s14, s12, 15
	s_add_u32 s13, s13, s14
	s_lshl_b32 s15, s3, 18
	s_lshl_b32 s28, s3, 12
	s_waitcnt lgkmcnt(0)
	s_add_u32 s16, s4, s13
	s_addc_u32 s17, s5, 0
	global_load_dwordx4 v[194:197], v226, s[16:17] offset:0 nt
	global_load_dwordx4 v[198:201], v226, s[16:17] offset:128 nt
	global_load_dwordx4 v[202:205], v226, s[16:17] offset:256 nt
	global_load_dwordx4 v[206:209], v226, s[16:17] offset:384 nt
	s_add_u32 s8, s8, s28
	s_addc_u32 s9, s9, 0
	global_load_dwordx2 v[238:239], v237, s[8:9]
	s_add_u32 s24, s6, s15
	s_addc_u32 s25, s7, 0
	s_add_u32 s32, s24, 0x1000
	s_addc_u32 s33, s25, 0
	s_add_u32 s34, s24, 0x2000
	s_addc_u32 s35, s25, 0
	s_add_u32 s36, s24, 0x3000
	s_addc_u32 s37, s25, 0
	s_add_u32 s38, s24, 0x4000
	s_addc_u32 s39, s25, 0
	s_add_u32 s40, s24, 0x5000
	s_addc_u32 s41, s25, 0
	s_add_u32 s42, s24, 0x6000
	s_addc_u32 s43, s25, 0
	s_add_u32 s44, s24, 0x7000
	s_addc_u32 s45, s25, 0
	global_load_dwordx4 v[34:37], v227, s[24:25] offset:0
	global_load_dwordx4 v[38:41], v227, s[24:25] offset:16
	global_load_dwordx4 v[26:29], v227, s[24:25] offset:2048
	global_load_dwordx4 v[30:33], v227, s[24:25] offset:2064
	global_load_dwordx4 v[50:53], v227, s[32:33] offset:0
	global_load_dwordx4 v[54:57], v227, s[32:33] offset:16
	global_load_dwordx4 v[42:45], v227, s[32:33] offset:2048
	global_load_dwordx4 v[46:49], v227, s[32:33] offset:2064
	global_load_dwordx4 v[18:21], v227, s[34:35] offset:0
	global_load_dwordx4 v[22:25], v227, s[34:35] offset:16
	global_load_dwordx4 v[130:133], v227, s[34:35] offset:2048
	global_load_dwordx4 v[134:137], v227, s[34:35] offset:2064
	global_load_dwordx4 v[122:125], v227, s[36:37] offset:0
	global_load_dwordx4 v[126:129], v227, s[36:37] offset:16
	global_load_dwordx4 v[138:141], v227, s[36:37] offset:2048
	global_load_dwordx4 v[142:145], v227, s[36:37] offset:2064
	global_load_dwordx4 v[98:101], v227, s[38:39] offset:0
	global_load_dwordx4 v[102:105], v227, s[38:39] offset:16
	global_load_dwordx4 v[90:93], v227, s[38:39] offset:2048
	global_load_dwordx4 v[94:97], v227, s[38:39] offset:2064
	global_load_dwordx4 v[114:117], v227, s[40:41] offset:0
	global_load_dwordx4 v[118:121], v227, s[40:41] offset:16
	global_load_dwordx4 v[106:109], v227, s[40:41] offset:2048
	global_load_dwordx4 v[110:113], v227, s[40:41] offset:2064
	global_load_dwordx4 v[58:61], v227, s[42:43] offset:0
	global_load_dwordx4 v[62:65], v227, s[42:43] offset:16
	global_load_dwordx4 v[66:69], v227, s[42:43] offset:2048
	global_load_dwordx4 v[70:73], v227, s[42:43] offset:2064
	global_load_dwordx4 v[74:77], v227, s[44:45] offset:0
	global_load_dwordx4 v[78:81], v227, s[44:45] offset:16
	global_load_dwordx4 v[82:85], v227, s[44:45] offset:2048
	global_load_dwordx4 v[86:89], v227, s[44:45] offset:2064
	s_add_u32 s18, s16, 0x100000
	s_addc_u32 s19, s17, 0
	s_add_u32 s20, s16, 0x200000
	s_addc_u32 s21, s17, 0
	s_add_u32 s22, s16, 0x300000
	s_addc_u32 s23, s17, 0
	v_mul_u32_u24_e32 v9, 0x110, v7
	v_lshl_add_u32 v9, v6, 7, v9
	v_lshl_add_u32 v228, v4, 4, v9
	v_lshlrev_b32_e32 v10, 6, v7
	v_lshl_or_b32 v10, v6, 5, v10
	v_lshl_or_b32 v229, v4, 2, v10
	v_and_b32_e32 v11, 31, v0
	v_bfe_u32 v12, v0, 5, 1
	v_mul_u32_u24_e32 v13, 0x110, v11
	v_lshl_add_u32 v230, v12, 5, v13
	v_lshlrev_b32_e32 v14, 9, v1
	v_lshl_or_b32 v231, v12, 4, v14
	v_xor_b32_e32 v15, 32, v2
	v_lshlrev_b32_e32 v232, 2, v15
	v_xor_b32_e32 v15, 16, v2
	v_lshlrev_b32_e32 v247, 2, v15
	v_lshlrev_b32_e32 v16, 7, v1
	v_lshl_or_b32 v233, v11, 2, v16
	v_mov_b32_e32 v234, 0x7f7f7f7f
	s_waitcnt vmcnt(32)
	ds_write_b64 v237, v[238:239] offset:34816
	v_mul_f32_e32 v244, v194, v194
	v_mul_f32_e32 v245, v198, v198
	v_cvt_pk_fp8_f32 v240, v194, v195
	v_cvt_pk_fp8_f32 v241, v198, v199
	v_cvt_pk_fp8_f32 v242, v202, v203
	v_cvt_pk_fp8_f32 v243, v206, v207
	v_fmac_f32_e32 v244, v195, v195
	v_fmac_f32_e32 v245, v199, v199
	v_fmac_f32_e32 v244, v196, v196
	v_fmac_f32_e32 v245, v200, v200
	v_fmac_f32_e32 v244, v197, v197
	v_fmac_f32_e32 v245, v201, v201
	v_fmac_f32_e32 v244, v202, v202
	v_fmac_f32_e32 v245, v206, v206
	v_fmac_f32_e32 v244, v203, v203
	v_fmac_f32_e32 v245, v207, v207
	v_fmac_f32_e32 v244, v204, v204
	v_fmac_f32_e32 v245, v208, v208
	v_fmac_f32_e32 v244, v205, v205
	v_fmac_f32_e32 v245, v209, v209
	v_cvt_pk_fp8_f32 v240, v196, v197 op_sel:[0,0,1]
	v_cvt_pk_fp8_f32 v241, v200, v201 op_sel:[0,0,1]
	v_cvt_pk_fp8_f32 v242, v204, v205 op_sel:[0,0,1]
	v_cvt_pk_fp8_f32 v243, v208, v209 op_sel:[0,0,1]
	v_add_f32_e32 v244, v244, v245
	s_nop 0
	ds_write_b128 v228, v[240:243] offset:0
	ds_write_b32 v229, v244 offset:38912
	global_load_dwordx4 v[210:213], v226, s[18:19] offset:0 nt
	global_load_dwordx4 v[214:217], v226, s[18:19] offset:128 nt
	global_load_dwordx4 v[218:221], v226, s[18:19] offset:256 nt
	global_load_dwordx4 v[222:225], v226, s[18:19] offset:384 nt
	s_waitcnt lgkmcnt(0)
	s_barrier
	ds_read_b128 v[162:165], v230 offset:0
	ds_read_b128 v[166:169], v230 offset:16
	ds_read_b128 v[2:5], v231 offset:34816
	ds_read_b128 v[6:9], v231 offset:34848
	ds_read_b128 v[10:13], v231 offset:34880
	ds_read_b128 v[14:17], v231 offset:34912
	ds_read_b128 v[170:173], v230 offset:64
	ds_read_b128 v[174:177], v230 offset:80
	ds_read_b128 v[178:181], v230 offset:128
	ds_read_b128 v[182:185], v230 offset:144
	ds_read_b128 v[186:189], v230 offset:192
	ds_read_b128 v[190:193], v230 offset:208
	s_waitcnt vmcnt(34) lgkmcnt(6)
	v_mfma_scale_f32_32x32x64_f8f6f4 v[2:17], v[34:41], v[162:169], v[2:17], v234, v234 op_sel_hi:[0,0,0]
	s_waitcnt vmcnt(32) lgkmcnt(4)
	v_mfma_scale_f32_32x32x64_f8f6f4 v[2:17], v[26:33], v[170:177], v[2:17], v234, v234 op_sel_hi:[0,0,0]
	ds_read_b128 v[146:149], v231 offset:34944
	ds_read_b128 v[150:153], v231 offset:34976
	ds_read_b128 v[154:157], v231 offset:35008
	ds_read_b128 v[158:161], v231 offset:35040
	s_waitcnt vmcnt(30) lgkmcnt(6)
	v_mfma_scale_f32_32x32x64_f8f6f4 v[2:17], v[50:57], v[178:185], v[2:17], v234, v234 op_sel_hi:[0,0,0]
	s_waitcnt vmcnt(28) lgkmcnt(4)
	v_mfma_scale_f32_32x32x64_f8f6f4 v[2:17], v[42:49], v[186:193], v[2:17], v234, v234 op_sel_hi:[0,0,0]
	s_waitcnt lgkmcnt(0)
	s_waitcnt vmcnt(26)
	v_mfma_scale_f32_32x32x64_f8f6f4 v[146:161], v[18:25], v[162:169], v[146:161], v234, v234 op_sel_hi:[0,0,0]
	s_waitcnt vmcnt(24)
	v_mfma_scale_f32_32x32x64_f8f6f4 v[146:161], v[130:137], v[170:177], v[146:161], v234, v234 op_sel_hi:[0,0,0]
	v_min3_f32 v2, v2, v3, v4
	v_min3_f32 v5, v5, v6, v7
	v_min3_f32 v8, v8, v9, v10
	v_min3_f32 v11, v11, v12, v13
	v_min3_f32 v14, v14, v15, v16
	v_min3_f32 v2, v2, v5, v8
	v_min3_f32 v11, v11, v14, v17
	v_min_f32_e32 v235, v2, v11
	ds_read_b128 v[2:5], v231 offset:35072
	ds_read_b128 v[6:9], v231 offset:35104
	ds_read_b128 v[10:13], v231 offset:35136
	ds_read_b128 v[14:17], v231 offset:35168
	s_waitcnt vmcnt(22)
	v_mfma_scale_f32_32x32x64_f8f6f4 v[146:161], v[122:129], v[178:185], v[146:161], v234, v234 op_sel_hi:[0,0,0]
	s_waitcnt vmcnt(20)
	v_mfma_scale_f32_32x32x64_f8f6f4 v[146:161], v[138:145], v[186:193], v[146:161], v234, v234 op_sel_hi:[0,0,0]
	s_waitcnt vmcnt(18) lgkmcnt(0)
	v_mfma_scale_f32_32x32x64_f8f6f4 v[2:17], v[98:105], v[162:169], v[2:17], v234, v234 op_sel_hi:[0,0,0]
	s_waitcnt vmcnt(16)
	v_mfma_scale_f32_32x32x64_f8f6f4 v[2:17], v[90:97], v[170:177], v[2:17], v234, v234 op_sel_hi:[0,0,0]
	v_min3_f32 v146, v146, v147, v148
	v_min3_f32 v149, v149, v150, v151
	v_min3_f32 v152, v152, v153, v154
	v_min3_f32 v155, v155, v156, v157
	v_min3_f32 v158, v158, v159, v160
	v_min3_f32 v146, v146, v149, v152
	v_min3_f32 v155, v155, v158, v161
	v_min3_f32 v235, v235, v146, v155
	ds_read_b128 v[146:149], v231 offset:35200
	ds_read_b128 v[150:153], v231 offset:35232
	ds_read_b128 v[154:157], v231 offset:35264
	ds_read_b128 v[158:161], v231 offset:35296
	s_waitcnt vmcnt(14)
	v_mfma_scale_f32_32x32x64_f8f6f4 v[2:17], v[114:121], v[178:185], v[2:17], v234, v234 op_sel_hi:[0,0,0]
	s_waitcnt vmcnt(12)
	v_mfma_scale_f32_32x32x64_f8f6f4 v[2:17], v[106:113], v[186:193], v[2:17], v234, v234 op_sel_hi:[0,0,0]
	s_waitcnt vmcnt(10) lgkmcnt(0)
	v_mfma_scale_f32_32x32x64_f8f6f4 v[146:161], v[58:65], v[162:169], v[146:161], v234, v234 op_sel_hi:[0,0,0]
	s_waitcnt vmcnt(8)
	v_mfma_scale_f32_32x32x64_f8f6f4 v[146:161], v[66:73], v[170:177], v[146:161], v234, v234 op_sel_hi:[0,0,0]
	v_min3_f32 v2, v2, v3, v4
	v_min3_f32 v5, v5, v6, v7
	v_min3_f32 v8, v8, v9, v10
	v_min3_f32 v11, v11, v12, v13
	v_min3_f32 v14, v14, v15, v16
	v_min3_f32 v2, v2, v5, v8
	v_min3_f32 v11, v11, v14, v17
	v_min3_f32 v235, v235, v2, v11
	ds_read_b128 v[2:5], v231 offset:34816
	ds_read_b128 v[6:9], v231 offset:34848
	ds_read_b128 v[10:13], v231 offset:34880
	ds_read_b128 v[14:17], v231 offset:34912
	s_waitcnt vmcnt(6)
	v_mfma_scale_f32_32x32x64_f8f6f4 v[146:161], v[74:81], v[178:185], v[146:161], v234, v234 op_sel_hi:[0,0,0]
	s_waitcnt vmcnt(4)
	v_mfma_scale_f32_32x32x64_f8f6f4 v[146:161], v[82:89], v[186:193], v[146:161], v234, v234 op_sel_hi:[0,0,0]
	s_waitcnt vmcnt(0)
	v_mul_f32_e32 v244, v210, v210
	v_mul_f32_e32 v245, v214, v214
	v_cvt_pk_fp8_f32 v240, v210, v211
	v_cvt_pk_fp8_f32 v241, v214, v215
	v_cvt_pk_fp8_f32 v242, v218, v219
	v_cvt_pk_fp8_f32 v243, v222, v223
	v_fmac_f32_e32 v244, v211, v211
	v_fmac_f32_e32 v245, v215, v215
	v_fmac_f32_e32 v244, v212, v212
	v_fmac_f32_e32 v245, v216, v216
	v_fmac_f32_e32 v244, v213, v213
	v_fmac_f32_e32 v245, v217, v217
	v_fmac_f32_e32 v244, v218, v218
	v_fmac_f32_e32 v245, v222, v222
	v_fmac_f32_e32 v244, v219, v219
	v_fmac_f32_e32 v245, v223, v223
	v_fmac_f32_e32 v244, v220, v220
	v_fmac_f32_e32 v245, v224, v224
	v_fmac_f32_e32 v244, v221, v221
	v_fmac_f32_e32 v245, v225, v225
	v_cvt_pk_fp8_f32 v240, v212, v213 op_sel:[0,0,1]
	v_cvt_pk_fp8_f32 v241, v216, v217 op_sel:[0,0,1]
	v_cvt_pk_fp8_f32 v242, v220, v221 op_sel:[0,0,1]
	v_cvt_pk_fp8_f32 v243, v224, v225 op_sel:[0,0,1]
	v_add_f32_e32 v244, v244, v245
	s_nop 0
	ds_write_b128 v228, v[240:243] offset:8704
	ds_write_b32 v229, v244 offset:40960
	s_waitcnt lgkmcnt(0)
	s_barrier
	ds_read_b128 v[162:165], v230 offset:8704
	ds_read_b128 v[166:169], v230 offset:8720
	ds_read_b128 v[170:173], v230 offset:8768
	ds_read_b128 v[174:177], v230 offset:8784
	ds_read_b128 v[178:181], v230 offset:8832
	ds_read_b128 v[182:185], v230 offset:8848
	ds_read_b128 v[186:189], v230 offset:8896
	ds_read_b128 v[190:193], v230 offset:8912
	s_waitcnt lgkmcnt(6)
	v_mfma_scale_f32_32x32x64_f8f6f4 v[2:17], v[34:41], v[162:169], v[2:17], v234, v234 op_sel_hi:[0,0,0]
	s_waitcnt lgkmcnt(4)
	v_mfma_scale_f32_32x32x64_f8f6f4 v[2:17], v[26:33], v[170:177], v[2:17], v234, v234 op_sel_hi:[0,0,0]
	v_min3_f32 v146, v146, v147, v148
	v_min3_f32 v149, v149, v150, v151
	v_min3_f32 v152, v152, v153, v154
	v_min3_f32 v155, v155, v156, v157
	v_min3_f32 v158, v158, v159, v160
	v_min3_f32 v146, v146, v149, v152
	v_min3_f32 v155, v155, v158, v161
	v_min3_f32 v235, v235, v146, v155
	ds_bpermute_b32 v246, v232, v235
	ds_read_b128 v[146:149], v231 offset:34944
	ds_read_b128 v[150:153], v231 offset:34976
	ds_read_b128 v[154:157], v231 offset:35008
	ds_read_b128 v[158:161], v231 offset:35040
	s_waitcnt lgkmcnt(7)
	v_mfma_scale_f32_32x32x64_f8f6f4 v[2:17], v[50:57], v[178:185], v[2:17], v234, v234 op_sel_hi:[0,0,0]
	s_waitcnt lgkmcnt(5)
	v_mfma_scale_f32_32x32x64_f8f6f4 v[2:17], v[42:49], v[186:193], v[2:17], v234, v234 op_sel_hi:[0,0,0]
	global_load_dwordx4 v[194:197], v226, s[20:21] offset:0 nt
	global_load_dwordx4 v[198:201], v226, s[20:21] offset:128 nt
	global_load_dwordx4 v[202:205], v226, s[20:21] offset:256 nt
	global_load_dwordx4 v[206:209], v226, s[20:21] offset:384 nt
	s_waitcnt lgkmcnt(0)
	v_min_f32_e32 v246, v235, v246
	ds_write_b32 v233, v246 offset:47104
	v_mfma_scale_f32_32x32x64_f8f6f4 v[146:161], v[18:25], v[162:169], v[146:161], v234, v234 op_sel_hi:[0,0,0]
	v_mfma_scale_f32_32x32x64_f8f6f4 v[146:161], v[130:137], v[170:177], v[146:161], v234, v234 op_sel_hi:[0,0,0]
	v_min3_f32 v2, v2, v3, v4
	v_min3_f32 v5, v5, v6, v7
	v_min3_f32 v8, v8, v9, v10
	v_min3_f32 v11, v11, v12, v13
	v_min3_f32 v14, v14, v15, v16
	v_min3_f32 v2, v2, v5, v8
	v_min3_f32 v11, v11, v14, v17
	v_min_f32_e32 v236, v2, v11
	ds_read_b128 v[2:5], v231 offset:35072
	ds_read_b128 v[6:9], v231 offset:35104
	ds_read_b128 v[10:13], v231 offset:35136
	ds_read_b128 v[14:17], v231 offset:35168
	v_mfma_scale_f32_32x32x64_f8f6f4 v[146:161], v[122:129], v[178:185], v[146:161], v234, v234 op_sel_hi:[0,0,0]
	v_mfma_scale_f32_32x32x64_f8f6f4 v[146:161], v[138:145], v[186:193], v[146:161], v234, v234 op_sel_hi:[0,0,0]
	s_waitcnt lgkmcnt(0)
	v_mfma_scale_f32_32x32x64_f8f6f4 v[2:17], v[98:105], v[162:169], v[2:17], v234, v234 op_sel_hi:[0,0,0]
	v_mfma_scale_f32_32x32x64_f8f6f4 v[2:17], v[90:97], v[170:177], v[2:17], v234, v234 op_sel_hi:[0,0,0]
	v_min3_f32 v146, v146, v147, v148
	v_min3_f32 v149, v149, v150, v151
	v_min3_f32 v152, v152, v153, v154
	v_min3_f32 v155, v155, v156, v157
	v_min3_f32 v158, v158, v159, v160
	v_min3_f32 v146, v146, v149, v152
	v_min3_f32 v155, v155, v158, v161
	v_min3_f32 v236, v236, v146, v155
	ds_read_b128 v[146:149], v231 offset:35200
	ds_read_b128 v[150:153], v231 offset:35232
	ds_read_b128 v[154:157], v231 offset:35264
	ds_read_b128 v[158:161], v231 offset:35296
	v_mfma_scale_f32_32x32x64_f8f6f4 v[2:17], v[114:121], v[178:185], v[2:17], v234, v234 op_sel_hi:[0,0,0]
	v_mfma_scale_f32_32x32x64_f8f6f4 v[2:17], v[106:113], v[186:193], v[2:17], v234, v234 op_sel_hi:[0,0,0]
	s_waitcnt lgkmcnt(0)
	v_mfma_scale_f32_32x32x64_f8f6f4 v[146:161], v[58:65], v[162:169], v[146:161], v234, v234 op_sel_hi:[0,0,0]
	v_mfma_scale_f32_32x32x64_f8f6f4 v[146:161], v[66:73], v[170:177], v[146:161], v234, v234 op_sel_hi:[0,0,0]
	v_min3_f32 v2, v2, v3, v4
	v_min3_f32 v5, v5, v6, v7
	v_min3_f32 v8, v8, v9, v10
	v_min3_f32 v11, v11, v12, v13
	v_min3_f32 v14, v14, v15, v16
	v_min3_f32 v2, v2, v5, v8
	v_min3_f32 v11, v11, v14, v17
	v_min3_f32 v236, v236, v2, v11
	ds_read_b128 v[2:5], v231 offset:34816
	ds_read_b128 v[6:9], v231 offset:34848
	ds_read_b128 v[10:13], v231 offset:34880
	ds_read_b128 v[14:17], v231 offset:34912
	v_mfma_scale_f32_32x32x64_f8f6f4 v[146:161], v[74:81], v[178:185], v[146:161], v234, v234 op_sel_hi:[0,0,0]
	v_mfma_scale_f32_32x32x64_f8f6f4 v[146:161], v[82:89], v[186:193], v[146:161], v234, v234 op_sel_hi:[0,0,0]
	s_waitcnt vmcnt(0)
	v_mul_f32_e32 v244, v194, v194
	v_mul_f32_e32 v245, v198, v198
	v_cvt_pk_fp8_f32 v240, v194, v195
	v_cvt_pk_fp8_f32 v241, v198, v199
	v_cvt_pk_fp8_f32 v242, v202, v203
	v_cvt_pk_fp8_f32 v243, v206, v207
	v_fmac_f32_e32 v244, v195, v195
	v_fmac_f32_e32 v245, v199, v199
	v_fmac_f32_e32 v244, v196, v196
	v_fmac_f32_e32 v245, v200, v200
	v_fmac_f32_e32 v244, v197, v197
	v_fmac_f32_e32 v245, v201, v201
	v_fmac_f32_e32 v244, v202, v202
	v_fmac_f32_e32 v245, v206, v206
	v_fmac_f32_e32 v244, v203, v203
	v_fmac_f32_e32 v245, v207, v207
	v_fmac_f32_e32 v244, v204, v204
	v_fmac_f32_e32 v245, v208, v208
	v_fmac_f32_e32 v244, v205, v205
	v_fmac_f32_e32 v245, v209, v209
	v_cvt_pk_fp8_f32 v240, v196, v197 op_sel:[0,0,1]
	v_cvt_pk_fp8_f32 v241, v200, v201 op_sel:[0,0,1]
	v_cvt_pk_fp8_f32 v242, v204, v205 op_sel:[0,0,1]
	v_cvt_pk_fp8_f32 v243, v208, v209 op_sel:[0,0,1]
	v_add_f32_e32 v244, v244, v245
	s_nop 0
	ds_write_b128 v228, v[240:243] offset:17408
	ds_write_b32 v229, v244 offset:43008
	s_waitcnt lgkmcnt(0)
	s_barrier
	ds_read_b128 v[162:165], v230 offset:17408
	ds_read_b128 v[166:169], v230 offset:17424
	ds_read_b128 v[170:173], v230 offset:17472
	ds_read_b128 v[174:177], v230 offset:17488
	ds_read_b128 v[178:181], v230 offset:17536
	ds_read_b128 v[182:185], v230 offset:17552
	ds_read_b128 v[186:189], v230 offset:17600
	ds_read_b128 v[190:193], v230 offset:17616
	s_waitcnt lgkmcnt(6)
	v_mfma_scale_f32_32x32x64_f8f6f4 v[2:17], v[34:41], v[162:169], v[2:17], v234, v234 op_sel_hi:[0,0,0]
	s_waitcnt lgkmcnt(4)
	v_mfma_scale_f32_32x32x64_f8f6f4 v[2:17], v[26:33], v[170:177], v[2:17], v234, v234 op_sel_hi:[0,0,0]
	v_min3_f32 v146, v146, v147, v148
	v_min3_f32 v149, v149, v150, v151
	v_min3_f32 v152, v152, v153, v154
	v_min3_f32 v155, v155, v156, v157
	v_min3_f32 v158, v158, v159, v160
	v_min3_f32 v146, v146, v149, v152
	v_min3_f32 v155, v155, v158, v161
	v_min3_f32 v236, v236, v146, v155
	ds_bpermute_b32 v246, v232, v236
	ds_read_b128 v[146:149], v231 offset:34944
	ds_read_b128 v[150:153], v231 offset:34976
	ds_read_b128 v[154:157], v231 offset:35008
	ds_read_b128 v[158:161], v231 offset:35040
	s_waitcnt lgkmcnt(7)
	v_mfma_scale_f32_32x32x64_f8f6f4 v[2:17], v[50:57], v[178:185], v[2:17], v234, v234 op_sel_hi:[0,0,0]
	s_waitcnt lgkmcnt(5)
	v_mfma_scale_f32_32x32x64_f8f6f4 v[2:17], v[42:49], v[186:193], v[2:17], v234, v234 op_sel_hi:[0,0,0]
	global_load_dwordx4 v[210:213], v226, s[22:23] offset:0 nt
	global_load_dwordx4 v[214:217], v226, s[22:23] offset:128 nt
	global_load_dwordx4 v[218:221], v226, s[22:23] offset:256 nt
	global_load_dwordx4 v[222:225], v226, s[22:23] offset:384 nt
	s_waitcnt lgkmcnt(0)
	v_min_f32_e32 v246, v236, v246
	ds_write_b32 v233, v246 offset:48128
	v_mfma_scale_f32_32x32x64_f8f6f4 v[146:161], v[18:25], v[162:169], v[146:161], v234, v234 op_sel_hi:[0,0,0]
	v_mfma_scale_f32_32x32x64_f8f6f4 v[146:161], v[130:137], v[170:177], v[146:161], v234, v234 op_sel_hi:[0,0,0]
	v_min3_f32 v2, v2, v3, v4
	v_min3_f32 v5, v5, v6, v7
	v_min3_f32 v8, v8, v9, v10
	v_min3_f32 v11, v11, v12, v13
	v_min3_f32 v14, v14, v15, v16
	v_min3_f32 v2, v2, v5, v8
	v_min3_f32 v11, v11, v14, v17
	v_min_f32_e32 v235, v2, v11
	ds_read_b128 v[2:5], v231 offset:35072
	ds_read_b128 v[6:9], v231 offset:35104
	ds_read_b128 v[10:13], v231 offset:35136
	ds_read_b128 v[14:17], v231 offset:35168
	v_mfma_scale_f32_32x32x64_f8f6f4 v[146:161], v[122:129], v[178:185], v[146:161], v234, v234 op_sel_hi:[0,0,0]
	v_mfma_scale_f32_32x32x64_f8f6f4 v[146:161], v[138:145], v[186:193], v[146:161], v234, v234 op_sel_hi:[0,0,0]
	s_waitcnt lgkmcnt(0)
	v_mfma_scale_f32_32x32x64_f8f6f4 v[2:17], v[98:105], v[162:169], v[2:17], v234, v234 op_sel_hi:[0,0,0]
	v_mfma_scale_f32_32x32x64_f8f6f4 v[2:17], v[90:97], v[170:177], v[2:17], v234, v234 op_sel_hi:[0,0,0]
	v_min3_f32 v146, v146, v147, v148
	v_min3_f32 v149, v149, v150, v151
	v_min3_f32 v152, v152, v153, v154
	v_min3_f32 v155, v155, v156, v157
	v_min3_f32 v158, v158, v159, v160
	v_min3_f32 v146, v146, v149, v152
	v_min3_f32 v155, v155, v158, v161
	v_min3_f32 v235, v235, v146, v155
	ds_read_b128 v[146:149], v231 offset:35200
	ds_read_b128 v[150:153], v231 offset:35232
	ds_read_b128 v[154:157], v231 offset:35264
	ds_read_b128 v[158:161], v231 offset:35296
	v_mfma_scale_f32_32x32x64_f8f6f4 v[2:17], v[114:121], v[178:185], v[2:17], v234, v234 op_sel_hi:[0,0,0]
	v_mfma_scale_f32_32x32x64_f8f6f4 v[2:17], v[106:113], v[186:193], v[2:17], v234, v234 op_sel_hi:[0,0,0]
	s_waitcnt lgkmcnt(0)
	v_mfma_scale_f32_32x32x64_f8f6f4 v[146:161], v[58:65], v[162:169], v[146:161], v234, v234 op_sel_hi:[0,0,0]
	v_mfma_scale_f32_32x32x64_f8f6f4 v[146:161], v[66:73], v[170:177], v[146:161], v234, v234 op_sel_hi:[0,0,0]
	v_min3_f32 v2, v2, v3, v4
	v_min3_f32 v5, v5, v6, v7
	v_min3_f32 v8, v8, v9, v10
	v_min3_f32 v11, v11, v12, v13
	v_min3_f32 v14, v14, v15, v16
	v_min3_f32 v2, v2, v5, v8
	v_min3_f32 v11, v11, v14, v17
	v_min3_f32 v235, v235, v2, v11
	ds_read_b128 v[2:5], v231 offset:34816
	ds_read_b128 v[6:9], v231 offset:34848
	ds_read_b128 v[10:13], v231 offset:34880
	ds_read_b128 v[14:17], v231 offset:34912
	v_mfma_scale_f32_32x32x64_f8f6f4 v[146:161], v[74:81], v[178:185], v[146:161], v234, v234 op_sel_hi:[0,0,0]
	v_mfma_scale_f32_32x32x64_f8f6f4 v[146:161], v[82:89], v[186:193], v[146:161], v234, v234 op_sel_hi:[0,0,0]
	s_waitcnt vmcnt(0)
	v_mul_f32_e32 v244, v210, v210
	v_mul_f32_e32 v245, v214, v214
	v_cvt_pk_fp8_f32 v240, v210, v211
	v_cvt_pk_fp8_f32 v241, v214, v215
	v_cvt_pk_fp8_f32 v242, v218, v219
	v_cvt_pk_fp8_f32 v243, v222, v223
	v_fmac_f32_e32 v244, v211, v211
	v_fmac_f32_e32 v245, v215, v215
	v_fmac_f32_e32 v244, v212, v212
	v_fmac_f32_e32 v245, v216, v216
	v_fmac_f32_e32 v244, v213, v213
	v_fmac_f32_e32 v245, v217, v217
	v_fmac_f32_e32 v244, v218, v218
	v_fmac_f32_e32 v245, v222, v222
	v_fmac_f32_e32 v244, v219, v219
	v_fmac_f32_e32 v245, v223, v223
	v_fmac_f32_e32 v244, v220, v220
	v_fmac_f32_e32 v245, v224, v224
	v_fmac_f32_e32 v244, v221, v221
	v_fmac_f32_e32 v245, v225, v225
	v_cvt_pk_fp8_f32 v240, v212, v213 op_sel:[0,0,1]
	v_cvt_pk_fp8_f32 v241, v216, v217 op_sel:[0,0,1]
	v_cvt_pk_fp8_f32 v242, v220, v221 op_sel:[0,0,1]
	v_cvt_pk_fp8_f32 v243, v224, v225 op_sel:[0,0,1]
	v_add_f32_e32 v244, v244, v245
	s_nop 0
	ds_write_b128 v228, v[240:243] offset:26112
	ds_write_b32 v229, v244 offset:45056
	s_waitcnt lgkmcnt(0)
	s_barrier
	ds_read_b128 v[162:165], v230 offset:26112
	ds_read_b128 v[166:169], v230 offset:26128
	ds_read_b128 v[170:173], v230 offset:26176
	ds_read_b128 v[174:177], v230 offset:26192
	ds_read_b128 v[178:181], v230 offset:26240
	ds_read_b128 v[182:185], v230 offset:26256
	ds_read_b128 v[186:189], v230 offset:26304
	ds_read_b128 v[190:193], v230 offset:26320
	s_waitcnt lgkmcnt(6)
	v_mfma_scale_f32_32x32x64_f8f6f4 v[2:17], v[34:41], v[162:169], v[2:17], v234, v234 op_sel_hi:[0,0,0]
	s_waitcnt lgkmcnt(4)
	v_mfma_scale_f32_32x32x64_f8f6f4 v[2:17], v[26:33], v[170:177], v[2:17], v234, v234 op_sel_hi:[0,0,0]
	v_min3_f32 v146, v146, v147, v148
	v_min3_f32 v149, v149, v150, v151
	v_min3_f32 v152, v152, v153, v154
	v_min3_f32 v155, v155, v156, v157
	v_min3_f32 v158, v158, v159, v160
	v_min3_f32 v146, v146, v149, v152
	v_min3_f32 v155, v155, v158, v161
	v_min3_f32 v235, v235, v146, v155
	ds_bpermute_b32 v246, v232, v235
	ds_read_b128 v[146:149], v231 offset:34944
	ds_read_b128 v[150:153], v231 offset:34976
	ds_read_b128 v[154:157], v231 offset:35008
	ds_read_b128 v[158:161], v231 offset:35040
	s_waitcnt lgkmcnt(7)
	v_mfma_scale_f32_32x32x64_f8f6f4 v[2:17], v[50:57], v[178:185], v[2:17], v234, v234 op_sel_hi:[0,0,0]
	s_waitcnt lgkmcnt(5)
	v_mfma_scale_f32_32x32x64_f8f6f4 v[2:17], v[42:49], v[186:193], v[2:17], v234, v234 op_sel_hi:[0,0,0]
	s_waitcnt lgkmcnt(0)
	v_min_f32_e32 v246, v235, v246
	ds_write_b32 v233, v246 offset:49152
	v_mfma_scale_f32_32x32x64_f8f6f4 v[146:161], v[18:25], v[162:169], v[146:161], v234, v234 op_sel_hi:[0,0,0]
	v_mfma_scale_f32_32x32x64_f8f6f4 v[146:161], v[130:137], v[170:177], v[146:161], v234, v234 op_sel_hi:[0,0,0]
	v_min3_f32 v2, v2, v3, v4
	v_min3_f32 v5, v5, v6, v7
	v_min3_f32 v8, v8, v9, v10
	v_min3_f32 v11, v11, v12, v13
	v_min3_f32 v14, v14, v15, v16
	v_min3_f32 v2, v2, v5, v8
	v_min3_f32 v11, v11, v14, v17
	v_min_f32_e32 v236, v2, v11
	ds_read_b128 v[2:5], v231 offset:35072
	ds_read_b128 v[6:9], v231 offset:35104
	ds_read_b128 v[10:13], v231 offset:35136
	ds_read_b128 v[14:17], v231 offset:35168
	v_mfma_scale_f32_32x32x64_f8f6f4 v[146:161], v[122:129], v[178:185], v[146:161], v234, v234 op_sel_hi:[0,0,0]
	v_mfma_scale_f32_32x32x64_f8f6f4 v[146:161], v[138:145], v[186:193], v[146:161], v234, v234 op_sel_hi:[0,0,0]
	s_waitcnt lgkmcnt(0)
	v_mfma_scale_f32_32x32x64_f8f6f4 v[2:17], v[98:105], v[162:169], v[2:17], v234, v234 op_sel_hi:[0,0,0]
	v_mfma_scale_f32_32x32x64_f8f6f4 v[2:17], v[90:97], v[170:177], v[2:17], v234, v234 op_sel_hi:[0,0,0]
	v_min3_f32 v146, v146, v147, v148
	v_min3_f32 v149, v149, v150, v151
	v_min3_f32 v152, v152, v153, v154
	v_min3_f32 v155, v155, v156, v157
	v_min3_f32 v158, v158, v159, v160
	v_min3_f32 v146, v146, v149, v152
	v_min3_f32 v155, v155, v158, v161
	v_min3_f32 v236, v236, v146, v155
	ds_read_b128 v[146:149], v231 offset:35200
	ds_read_b128 v[150:153], v231 offset:35232
	ds_read_b128 v[154:157], v231 offset:35264
	ds_read_b128 v[158:161], v231 offset:35296
	v_mfma_scale_f32_32x32x64_f8f6f4 v[2:17], v[114:121], v[178:185], v[2:17], v234, v234 op_sel_hi:[0,0,0]
	v_mfma_scale_f32_32x32x64_f8f6f4 v[2:17], v[106:113], v[186:193], v[2:17], v234, v234 op_sel_hi:[0,0,0]
	s_waitcnt lgkmcnt(0)
	v_mfma_scale_f32_32x32x64_f8f6f4 v[146:161], v[58:65], v[162:169], v[146:161], v234, v234 op_sel_hi:[0,0,0]
	v_mfma_scale_f32_32x32x64_f8f6f4 v[146:161], v[66:73], v[170:177], v[146:161], v234, v234 op_sel_hi:[0,0,0]
	v_min3_f32 v2, v2, v3, v4
	v_min3_f32 v5, v5, v6, v7
	v_min3_f32 v8, v8, v9, v10
	v_min3_f32 v11, v11, v12, v13
	v_min3_f32 v14, v14, v15, v16
	v_min3_f32 v2, v2, v5, v8
	v_min3_f32 v11, v11, v14, v17
	v_min3_f32 v236, v236, v2, v11
	v_mfma_scale_f32_32x32x64_f8f6f4 v[146:161], v[74:81], v[178:185], v[146:161], v234, v234 op_sel_hi:[0,0,0]
	v_mfma_scale_f32_32x32x64_f8f6f4 v[146:161], v[82:89], v[186:193], v[146:161], v234, v234 op_sel_hi:[0,0,0]
	v_cmp_gt_u32_e32 vcc, 0x80, v0
	s_and_saveexec_b64 s[34:35], vcc
	v_lshlrev_b32_e32 v36, 6, v0
	ds_read_b128 v[20:23], v36 offset:38912
	ds_read_b128 v[24:27], v36 offset:38928
	ds_read_b128 v[28:31], v36 offset:38944
	ds_read_b128 v[32:35], v36 offset:38960
	s_mov_b64 exec, s[34:35]
	s_nop 15
	s_nop 3
	v_min3_f32 v146, v146, v147, v148
	v_min3_f32 v149, v149, v150, v151
	v_min3_f32 v152, v152, v153, v154
	v_min3_f32 v155, v155, v156, v157
	v_min3_f32 v158, v158, v159, v160
	v_min3_f32 v146, v146, v149, v152
	v_min3_f32 v155, v155, v158, v161
	v_min3_f32 v236, v236, v146, v155
	ds_bpermute_b32 v246, v232, v236
	s_waitcnt lgkmcnt(0)
	v_min_f32_e32 v246, v236, v246
	ds_write_b32 v233, v246 offset:50176
	s_waitcnt lgkmcnt(0)
	s_barrier
	v_readfirstlane_b32 s2, v1
	s_nop 3
	s_cmp_gt_u32 s2, 1
	s_cbranch_scc1 .Lmain_end
	v_and_b32_e32 v2, 31, v0
	v_lshlrev_b32_e32 v3, 5, v0
	v_and_b32_e32 v3, 0xc00, v3
	v_lshl_or_b32 v8, v2, 2, v3
	v_add_u32_e32 v8, 0xb800, v8
	ds_read2_b32 v[2:3], v8 offset1:32
	ds_read2_b32 v[4:5], v8 offset0:64 offset1:96
	ds_read2_b32 v[6:7], v8 offset0:128 offset1:160
	ds_read2_b32 v[10:11], v8 offset0:192 offset1:224
	s_mov_b32 s8, 0xf800000
	s_lshr_b32 s2, s30, 3
	s_lshl_b32 s2, s2, 7
	s_add_u32 s2, s2, 0x300000
	s_add_u32 s6, s6, s2
	s_addc_u32 s7, s7, 0
	s_mov_b32 s4, 0
	s_mov_b32 s5, 0x41d00000
	s_mov_b32 s16, 0
	s_mov_b32 s17, 0x420e0000
	s_waitcnt lgkmcnt(0)
	v_min3_f32 v2, v2, v3, v4
	v_min3_f32 v5, v5, v6, v7
	v_min3_f32 v2, v2, v10, v11
	v_min_f32_e32 v2, v2, v5
	s_waitcnt lgkmcnt(0)
	v_add_f32_e32 v20, v20, v21
	v_add_f32_e32 v22, v22, v23
	v_add_f32_e32 v24, v24, v25
	v_add_f32_e32 v26, v26, v27
	v_add_f32_e32 v28, v28, v29
	v_add_f32_e32 v30, v30, v31
	v_add_f32_e32 v32, v32, v33
	v_add_f32_e32 v34, v34, v35
	v_add_f32_e32 v20, v20, v22
	v_add_f32_e32 v24, v24, v26
	v_add_f32_e32 v28, v28, v30
	v_add_f32_e32 v32, v32, v34
	v_add_f32_e32 v20, v20, v24
	v_add_f32_e32 v28, v28, v32
	v_add_f32_e32 v20, v20, v28
	v_add_f32_e32 v2, v2, v20
	v_max_f32_e32 v2, 0, v2
	v_mul_f32_e32 v3, 0x4f800000, v2
	v_cmp_gt_f32_e32 vcc, s8, v2
	s_nop 1
	v_cndmask_b32_e32 v2, v2, v3, vcc
	v_sqrt_f32_e32 v3, v2
	s_nop 0
	v_add_u32_e32 v4, -1, v3
	v_fma_f32 v5, -v4, v3, v2
	v_cmp_ge_f32_e64 s[18:19], 0, v5
	v_add_u32_e32 v5, 1, v3
	s_nop 0
	v_cndmask_b32_e64 v4, v3, v4, s[18:19]
	v_fma_f32 v3, -v5, v3, v2
	v_cmp_lt_f32_e64 s[18:19], 0, v3
	s_nop 1
	v_cndmask_b32_e64 v3, v4, v5, s[18:19]
	v_mul_f32_e32 v4, 0x37800000, v3
	v_cndmask_b32_e32 v3, v3, v4, vcc
	v_mov_b32_e32 v4, 0x260
	v_cmp_class_f32_e32 vcc, v2, v4
	s_nop 1
	v_cndmask_b32_e32 v2, v3, v2, vcc
	s_nop 1
	v_add_f32_dpp v3, v2, v2 quad_perm:[1,0,3,2] row_mask:0xf bank_mask:0xf
	s_nop 1
	v_add_f32_dpp v4, v3, v3 quad_perm:[2,3,0,1] row_mask:0xf bank_mask:0xf
	s_nop 1
	v_add_f32_dpp v5, v4, v4 row_half_mirror row_mask:0xf bank_mask:0xf
	s_nop 1
	v_add_f32_dpp v6, v5, v5 row_mirror row_mask:0xf bank_mask:0xf
	s_nop 1
	v_readlane_b32 s12, v6, 0
	v_readlane_b32 s13, v6, 16
	v_readlane_b32 s14, v6, 32
	v_readlane_b32 s15, v6, 48
	s_nop 3
	v_mov_b32_e32 v7, s12
	v_add_f32_e32 v7, s13, v7
	v_mov_b32_e32 v9, s14
	v_add_f32_e32 v9, s15, v9
	v_add_f32_e32 v0, v7, v9
	v_mov_b32_e32 v4, 0
	s_mov_b64 exec, 1
	v_cvt_f64_f32_e32 v[6:7], v0
	v_add_f64 v[8:9], v[6:7], s[4:5]
	global_atomic_add_f64 v[10:11], v4, v[8:9], s[6:7] sc0
	s_waitcnt vmcnt(0)
	v_cmp_le_f64_e32 vcc, s[16:17], v[10:11]
	s_and_saveexec_b64 s[2:3], vcc
	s_cbranch_execz .Lmain_end
	v_add_f64 v[10:11], v[10:11], -s[16:17]
	v_add_f64 v[10:11], v[10:11], v[6:7]
	v_cvt_f32_f64_e32 v0, v[10:11]
	v_mul_f32_e32 v0, 0x38000000, v0
	global_atomic_add_f32 v4, v0, s[10:11]
